# router: norm gain vector loaded once per phase (was 8 serialized load+wait per 16-token batch); logits MFMA fragment reads software-pipelined (8 ds_reads in flight, counted lgkmcnt)
# speedup vs baseline: 1.0412x; 1.0036x over previous
.LBB0_476:
	s_cmpk_gt_i32 s72, 0xff
	s_cbranch_scc1 .LBB0_491
	s_load_dwordx4 s[40:43], s[0:1], 0x58
	s_load_dwordx2 s[38:39], s[0:1], 0x50
	s_load_dwordx2 s[26:27], s[0:1], 0x98
	s_ashr_i32 s83, s82, 31
	s_waitcnt vmcnt(0)
	v_ashrrev_i32_e32 v87, 5, v194
	v_readlane_b32 s6, v253, 16
	s_lshl_b64 s[4:5], s[82:83], 17
	s_waitcnt lgkmcnt(0)
	s_add_u32 s4, s40, s4
	v_lshl_add_u32 v4, v87, 3, s6
	v_and_b32_e32 v82, 31, v194
	v_add_u32_e32 v12, 0x73, v4
	s_addc_u32 s5, s41, s5
	v_lshlrev_b32_e32 v0, 2, v82
	v_ashrrev_i32_e32 v13, 31, v12
	v_lshl_add_u64 v[2:3], s[4:5], 0, v[0:1]
	v_lshlrev_b64 v[12:13], 7, v[12:13]
	v_lshl_add_u64 v[16:17], v[2:3], 0, v[12:13]
	v_add_u32_e32 v12, 0x74, v4
	v_ashrrev_i32_e32 v13, 31, v12
	v_lshlrev_b64 v[12:13], 7, v[12:13]
	v_lshl_add_u64 v[18:19], v[2:3], 0, v[12:13]
	v_add_u32_e32 v12, 0x75, v4
	v_ashrrev_i32_e32 v13, 31, v12
	v_lshlrev_b64 v[12:13], 7, v[12:13]
	v_lshl_add_u64 v[20:21], v[2:3], 0, v[12:13]
	v_add_u32_e32 v12, 0x76, v4
	s_lshl_b32 s14, s82, 5
	v_ashrrev_i32_e32 v13, 31, v12
	s_ashr_i32 s15, s14, 31
	v_add_u32_e32 v6, 0x70, v4
	v_add_u32_e32 v8, 0x71, v4
	v_add_u32_e32 v10, 0x72, v4
	v_lshlrev_b64 v[12:13], 7, v[12:13]
	s_lshl_b64 s[14:15], s[14:15], 2
	v_ashrrev_i32_e32 v7, 31, v6
	v_ashrrev_i32_e32 v9, 31, v8
	v_ashrrev_i32_e32 v11, 31, v10
	v_lshl_add_u64 v[22:23], v[2:3], 0, v[12:13]
	v_add_u32_e32 v12, 0x77, v4
	s_add_u32 s14, s42, s14
	v_lshlrev_b64 v[6:7], 7, v[6:7]
	v_lshlrev_b64 v[8:9], 7, v[8:9]
	v_lshlrev_b64 v[10:11], 7, v[10:11]
	v_ashrrev_i32_e32 v13, 31, v12
	s_addc_u32 s15, s43, s15
	v_lshl_add_u64 v[6:7], v[2:3], 0, v[6:7]
	v_lshl_add_u64 v[8:9], v[2:3], 0, v[8:9]
	v_lshl_add_u64 v[10:11], v[2:3], 0, v[10:11]
	v_lshlrev_b64 v[12:13], 7, v[12:13]
	global_load_dword v83, v0, s[14:15]
	v_lshl_add_u64 v[24:25], v[2:3], 0, v[12:13]
	global_load_dword v14, v[6:7], off
	global_load_dword v15, v[8:9], off
	global_load_dword v12, v[10:11], off
	global_load_dword v13, v[16:17], off
	s_nop 0
	global_load_dword v10, v[18:19], off
	global_load_dword v11, v[20:21], off
	global_load_dword v8, v[22:23], off
	global_load_dword v9, v[24:25], off
	v_add_u32_e32 v6, 0x60, v4
	v_add_u32_e32 v16, 0x61, v4
	v_ashrrev_i32_e32 v7, 31, v6
	v_ashrrev_i32_e32 v17, 31, v16
	v_add_u32_e32 v18, 0x62, v4
	v_add_u32_e32 v20, 0x63, v4
	v_add_u32_e32 v22, 0x64, v4
	v_add_u32_e32 v24, 0x65, v4
	v_add_u32_e32 v26, 0x66, v4
	v_add_u32_e32 v28, 0x67, v4
	v_lshlrev_b64 v[6:7], 7, v[6:7]
	v_lshlrev_b64 v[16:17], 7, v[16:17]
	v_ashrrev_i32_e32 v19, 31, v18
	v_ashrrev_i32_e32 v21, 31, v20
	v_ashrrev_i32_e32 v23, 31, v22
	v_ashrrev_i32_e32 v25, 31, v24
	v_ashrrev_i32_e32 v27, 31, v26
	v_ashrrev_i32_e32 v29, 31, v28
	v_lshl_add_u64 v[6:7], v[2:3], 0, v[6:7]
	v_lshl_add_u64 v[16:17], v[2:3], 0, v[16:17]
	v_lshlrev_b64 v[18:19], 7, v[18:19]
	v_lshlrev_b64 v[20:21], 7, v[20:21]
	v_lshlrev_b64 v[22:23], 7, v[22:23]
	v_lshlrev_b64 v[24:25], 7, v[24:25]
	v_lshlrev_b64 v[26:27], 7, v[26:27]
	v_lshlrev_b64 v[28:29], 7, v[28:29]
	v_lshl_add_u64 v[18:19], v[2:3], 0, v[18:19]
	v_lshl_add_u64 v[20:21], v[2:3], 0, v[20:21]
	v_lshl_add_u64 v[22:23], v[2:3], 0, v[22:23]
	v_lshl_add_u64 v[24:25], v[2:3], 0, v[24:25]
	v_lshl_add_u64 v[26:27], v[2:3], 0, v[26:27]
	v_lshl_add_u64 v[28:29], v[2:3], 0, v[28:29]
	global_load_dword v30, v[6:7], off
	global_load_dword v31, v[16:17], off
	global_load_dword v34, v[18:19], off
	global_load_dword v35, v[20:21], off
	global_load_dword v32, v[22:23], off
	global_load_dword v33, v[24:25], off
	s_nop 0
	global_load_dword v16, v[26:27], off
	global_load_dword v17, v[28:29], off
	v_add_u32_e32 v6, 0x50, v4
	v_ashrrev_i32_e32 v7, 31, v6
	v_add_u32_e32 v18, 0x51, v4
	v_add_u32_e32 v20, 0x52, v4
	v_add_u32_e32 v22, 0x53, v4
	v_add_u32_e32 v24, 0x54, v4
	v_add_u32_e32 v26, 0x55, v4
	v_add_u32_e32 v28, 0x56, v4
	v_add_u32_e32 v36, 0x57, v4
	v_lshlrev_b64 v[6:7], 7, v[6:7]
	v_ashrrev_i32_e32 v19, 31, v18
	v_ashrrev_i32_e32 v21, 31, v20
	v_ashrrev_i32_e32 v23, 31, v22
	v_ashrrev_i32_e32 v25, 31, v24
	v_ashrrev_i32_e32 v27, 31, v26
	v_ashrrev_i32_e32 v29, 31, v28
	v_ashrrev_i32_e32 v37, 31, v36
	v_lshl_add_u64 v[6:7], v[2:3], 0, v[6:7]
	v_lshlrev_b64 v[18:19], 7, v[18:19]
	v_lshlrev_b64 v[20:21], 7, v[20:21]
	v_lshlrev_b64 v[22:23], 7, v[22:23]
	v_lshlrev_b64 v[24:25], 7, v[24:25]
	v_lshlrev_b64 v[26:27], 7, v[26:27]
	v_lshlrev_b64 v[28:29], 7, v[28:29]
	v_lshlrev_b64 v[36:37], 7, v[36:37]
	v_lshl_add_u64 v[18:19], v[2:3], 0, v[18:19]
	v_lshl_add_u64 v[20:21], v[2:3], 0, v[20:21]
	v_lshl_add_u64 v[22:23], v[2:3], 0, v[22:23]
	v_lshl_add_u64 v[24:25], v[2:3], 0, v[24:25]
	v_lshl_add_u64 v[26:27], v[2:3], 0, v[26:27]
	v_lshl_add_u64 v[28:29], v[2:3], 0, v[28:29]
	v_lshl_add_u64 v[36:37], v[2:3], 0, v[36:37]
	global_load_dword v38, v[6:7], off
	global_load_dword v39, v[18:19], off
	global_load_dword v40, v[20:21], off
	global_load_dword v41, v[22:23], off
	global_load_dword v42, v[24:25], off
	global_load_dword v43, v[26:27], off
	global_load_dword v44, v[28:29], off
	global_load_dword v45, v[36:37], off
	v_add_u32_e32 v6, 64, v4
	v_ashrrev_i32_e32 v7, 31, v6
	v_add_u32_e32 v18, 0x41, v4
	v_lshlrev_b64 v[6:7], 7, v[6:7]
	v_ashrrev_i32_e32 v19, 31, v18
	v_lshl_add_u64 v[6:7], v[2:3], 0, v[6:7]
	v_lshlrev_b64 v[18:19], 7, v[18:19]
	v_lshl_add_u64 v[18:19], v[2:3], 0, v[18:19]
	global_load_dword v46, v[6:7], off
	global_load_dword v47, v[18:19], off
	v_add_u32_e32 v6, 0x42, v4
	v_ashrrev_i32_e32 v7, 31, v6
	v_add_u32_e32 v18, 0x43, v4
	v_add_u32_e32 v20, 0x44, v4
	v_add_u32_e32 v22, 0x45, v4
	v_lshlrev_b64 v[6:7], 7, v[6:7]
	v_ashrrev_i32_e32 v19, 31, v18
	v_ashrrev_i32_e32 v21, 31, v20
	v_ashrrev_i32_e32 v23, 31, v22
	v_lshl_add_u64 v[6:7], v[2:3], 0, v[6:7]
	v_lshlrev_b64 v[18:19], 7, v[18:19]
	v_lshlrev_b64 v[20:21], 7, v[20:21]
	v_lshlrev_b64 v[22:23], 7, v[22:23]
	v_lshl_add_u64 v[18:19], v[2:3], 0, v[18:19]
	v_lshl_add_u64 v[20:21], v[2:3], 0, v[20:21]
	v_lshl_add_u64 v[22:23], v[2:3], 0, v[22:23]
	global_load_dword v48, v[6:7], off
	global_load_dword v49, v[18:19], off
	global_load_dword v50, v[20:21], off
	global_load_dword v51, v[22:23], off
	v_add_u32_e32 v6, 0x46, v4
	v_add_u32_e32 v18, 0x47, v4
	v_ashrrev_i32_e32 v7, 31, v6
	v_ashrrev_i32_e32 v19, 31, v18
	v_lshlrev_b64 v[6:7], 7, v[6:7]
	v_lshlrev_b64 v[18:19], 7, v[18:19]
	v_lshl_add_u64 v[6:7], v[2:3], 0, v[6:7]
	v_lshl_add_u64 v[18:19], v[2:3], 0, v[18:19]
	global_load_dword v6, v[6:7], off
	s_nop 0
	global_load_dword v7, v[18:19], off
	s_waitcnt vmcnt(30)
	v_cvt_pk_bf16_f32 v18, v14, v15
	v_lshlrev_b32_e32 v20, 16, v18
	v_and_b32_e32 v21, 0xffff0000, v18
	v_pk_add_f32 v[14:15], v[14:15], v[20:21] neg_lo:[0,1] neg_hi:[0,1]
	s_waitcnt vmcnt(28)
	v_cvt_pk_bf16_f32 v19, v12, v13
	v_cvt_pk_bf16_f32 v22, v14, v15
	v_lshlrev_b32_e32 v14, 16, v19
	v_and_b32_e32 v15, 0xffff0000, v19
	v_pk_add_f32 v[12:13], v[12:13], v[14:15] neg_lo:[0,1] neg_hi:[0,1]
	s_waitcnt vmcnt(26)
	v_cvt_pk_bf16_f32 v20, v10, v11
	v_cvt_pk_bf16_f32 v23, v12, v13
	v_lshlrev_b32_e32 v12, 16, v20
	v_and_b32_e32 v13, 0xffff0000, v20
	v_pk_add_f32 v[10:11], v[10:11], v[12:13] neg_lo:[0,1] neg_hi:[0,1]
	s_waitcnt vmcnt(24)
	v_cvt_pk_bf16_f32 v21, v8, v9
	v_cvt_pk_bf16_f32 v24, v10, v11
	v_lshlrev_b32_e32 v10, 16, v21
	v_and_b32_e32 v11, 0xffff0000, v21
	v_pk_add_f32 v[8:9], v[8:9], v[10:11] neg_lo:[0,1] neg_hi:[0,1]
	s_waitcnt vmcnt(22)
	v_cvt_pk_bf16_f32 v26, v30, v31
	v_cvt_pk_bf16_f32 v25, v8, v9
	v_lshlrev_b32_e32 v8, 16, v26
	v_and_b32_e32 v9, 0xffff0000, v26
	v_pk_add_f32 v[8:9], v[30:31], v[8:9] neg_lo:[0,1] neg_hi:[0,1]
	s_waitcnt vmcnt(20)
	v_cvt_pk_bf16_f32 v27, v34, v35
	v_cvt_pk_bf16_f32 v30, v8, v9
	v_lshlrev_b32_e32 v8, 16, v27
	v_and_b32_e32 v9, 0xffff0000, v27
	v_pk_add_f32 v[8:9], v[34:35], v[8:9] neg_lo:[0,1] neg_hi:[0,1]
	s_waitcnt vmcnt(18)
	v_cvt_pk_bf16_f32 v28, v32, v33
	v_cvt_pk_bf16_f32 v31, v8, v9
	v_lshlrev_b32_e32 v8, 16, v28
	v_and_b32_e32 v9, 0xffff0000, v28
	v_pk_add_f32 v[8:9], v[32:33], v[8:9] neg_lo:[0,1] neg_hi:[0,1]
	s_waitcnt vmcnt(16)
	v_cvt_pk_bf16_f32 v29, v16, v17
	v_cvt_pk_bf16_f32 v32, v8, v9
	v_lshlrev_b32_e32 v8, 16, v29
	v_and_b32_e32 v9, 0xffff0000, v29
	v_pk_add_f32 v[8:9], v[16:17], v[8:9] neg_lo:[0,1] neg_hi:[0,1]
	s_waitcnt vmcnt(14)
	v_cvt_pk_bf16_f32 v34, v38, v39
	v_cvt_pk_bf16_f32 v33, v8, v9
	v_lshlrev_b32_e32 v8, 16, v34
	v_and_b32_e32 v9, 0xffff0000, v34
	v_pk_add_f32 v[8:9], v[38:39], v[8:9] neg_lo:[0,1] neg_hi:[0,1]
	s_waitcnt vmcnt(12)
	v_cvt_pk_bf16_f32 v35, v40, v41
	v_cvt_pk_bf16_f32 v38, v8, v9
	v_lshlrev_b32_e32 v8, 16, v35
	v_and_b32_e32 v9, 0xffff0000, v35
	v_pk_add_f32 v[8:9], v[40:41], v[8:9] neg_lo:[0,1] neg_hi:[0,1]
	s_waitcnt vmcnt(10)
	v_cvt_pk_bf16_f32 v36, v42, v43
	v_cvt_pk_bf16_f32 v39, v8, v9
	v_lshlrev_b32_e32 v8, 16, v36
	v_and_b32_e32 v9, 0xffff0000, v36
	v_pk_add_f32 v[8:9], v[42:43], v[8:9] neg_lo:[0,1] neg_hi:[0,1]
	s_waitcnt vmcnt(8)
	v_cvt_pk_bf16_f32 v37, v44, v45
	v_cvt_pk_bf16_f32 v40, v8, v9
	v_lshlrev_b32_e32 v8, 16, v37
	v_and_b32_e32 v9, 0xffff0000, v37
	v_pk_add_f32 v[8:9], v[44:45], v[8:9] neg_lo:[0,1] neg_hi:[0,1]
	s_waitcnt vmcnt(6)
	v_cvt_pk_bf16_f32 v42, v46, v47
	v_add_u32_e32 v14, 51, v4
	v_cvt_pk_bf16_f32 v41, v8, v9
	v_lshlrev_b32_e32 v8, 16, v42
	v_and_b32_e32 v9, 0xffff0000, v42
	v_ashrrev_i32_e32 v15, 31, v14
	v_pk_add_f32 v[8:9], v[46:47], v[8:9] neg_lo:[0,1] neg_hi:[0,1]
	v_lshlrev_b64 v[14:15], 7, v[14:15]
	v_cvt_pk_bf16_f32 v46, v8, v9
	s_waitcnt vmcnt(4)
	v_cvt_pk_bf16_f32 v43, v48, v49
	v_lshlrev_b32_e32 v8, 16, v43
	v_and_b32_e32 v9, 0xffff0000, v43
	v_lshl_add_u64 v[16:17], v[2:3], 0, v[14:15]
	v_add_u32_e32 v14, 52, v4
	v_pk_add_f32 v[8:9], v[48:49], v[8:9] neg_lo:[0,1] neg_hi:[0,1]
	s_waitcnt vmcnt(2)
	v_cvt_pk_bf16_f32 v44, v50, v51
	v_ashrrev_i32_e32 v15, 31, v14
	v_cvt_pk_bf16_f32 v47, v8, v9
	v_lshlrev_b32_e32 v8, 16, v44
	v_and_b32_e32 v9, 0xffff0000, v44
	v_lshlrev_b64 v[14:15], 7, v[14:15]
	v_pk_add_f32 v[8:9], v[50:51], v[8:9] neg_lo:[0,1] neg_hi:[0,1]
	v_lshl_add_u64 v[50:51], v[2:3], 0, v[14:15]
	v_add_u32_e32 v14, 53, v4
	v_ashrrev_i32_e32 v15, 31, v14
	v_lshlrev_b64 v[14:15], 7, v[14:15]
	v_lshl_add_u64 v[52:53], v[2:3], 0, v[14:15]
	v_add_u32_e32 v14, 54, v4
	v_ashrrev_i32_e32 v15, 31, v14
	v_cvt_pk_bf16_f32 v48, v8, v9
	v_add_u32_e32 v8, 48, v4
	v_add_u32_e32 v10, 49, v4
	v_add_u32_e32 v12, 50, v4
	v_lshlrev_b64 v[14:15], 7, v[14:15]
	v_ashrrev_i32_e32 v9, 31, v8
	v_ashrrev_i32_e32 v11, 31, v10
	v_ashrrev_i32_e32 v13, 31, v12
	v_lshl_add_u64 v[54:55], v[2:3], 0, v[14:15]
	v_add_u32_e32 v14, 55, v4
	v_lshlrev_b64 v[8:9], 7, v[8:9]
	v_lshlrev_b64 v[10:11], 7, v[10:11]
	v_lshlrev_b64 v[12:13], 7, v[12:13]
	v_ashrrev_i32_e32 v15, 31, v14
	v_lshl_add_u64 v[8:9], v[2:3], 0, v[8:9]
	v_lshl_add_u64 v[10:11], v[2:3], 0, v[10:11]
	v_lshl_add_u64 v[12:13], v[2:3], 0, v[12:13]
	v_lshlrev_b64 v[14:15], 7, v[14:15]
	v_lshl_add_u64 v[56:57], v[2:3], 0, v[14:15]
	global_load_dword v14, v[8:9], off
	global_load_dword v15, v[10:11], off
	s_nop 0
	global_load_dword v12, v[12:13], off
	s_nop 0
	global_load_dword v13, v[16:17], off
	global_load_dword v10, v[50:51], off
	global_load_dword v11, v[52:53], off
	global_load_dword v8, v[54:55], off
	global_load_dword v9, v[56:57], off
	v_add_u32_e32 v16, 32, v4
	v_ashrrev_i32_e32 v17, 31, v16
	v_add_u32_e32 v50, 33, v4
	v_add_u32_e32 v52, 34, v4
	v_add_u32_e32 v54, 35, v4
	v_add_u32_e32 v56, 36, v4
	v_add_u32_e32 v58, 37, v4
	v_add_u32_e32 v60, 38, v4
	v_add_u32_e32 v62, 39, v4
	v_lshlrev_b64 v[16:17], 7, v[16:17]
	v_ashrrev_i32_e32 v51, 31, v50
	v_ashrrev_i32_e32 v53, 31, v52
	v_ashrrev_i32_e32 v55, 31, v54
	v_ashrrev_i32_e32 v57, 31, v56
	v_ashrrev_i32_e32 v59, 31, v58
	v_ashrrev_i32_e32 v61, 31, v60
	v_ashrrev_i32_e32 v63, 31, v62
	v_lshl_add_u64 v[16:17], v[2:3], 0, v[16:17]
	v_lshlrev_b64 v[50:51], 7, v[50:51]
	v_lshlrev_b64 v[52:53], 7, v[52:53]
	v_lshlrev_b64 v[54:55], 7, v[54:55]
	v_lshlrev_b64 v[56:57], 7, v[56:57]
	v_lshlrev_b64 v[58:59], 7, v[58:59]
	v_lshlrev_b64 v[60:61], 7, v[60:61]
	v_lshlrev_b64 v[62:63], 7, v[62:63]
	v_lshl_add_u64 v[50:51], v[2:3], 0, v[50:51]
	v_lshl_add_u64 v[52:53], v[2:3], 0, v[52:53]
	v_lshl_add_u64 v[54:55], v[2:3], 0, v[54:55]
	v_lshl_add_u64 v[56:57], v[2:3], 0, v[56:57]
	v_lshl_add_u64 v[58:59], v[2:3], 0, v[58:59]
	v_lshl_add_u64 v[60:61], v[2:3], 0, v[60:61]
	v_lshl_add_u64 v[62:63], v[2:3], 0, v[62:63]
	global_load_dword v64, v[16:17], off
	global_load_dword v65, v[50:51], off
	global_load_dword v66, v[52:53], off
	global_load_dword v67, v[54:55], off
	global_load_dword v68, v[56:57], off
	global_load_dword v69, v[58:59], off
	global_load_dword v16, v[60:61], off
	global_load_dword v17, v[62:63], off
	v_add_u32_e32 v50, 16, v4
	v_add_u32_e32 v52, 17, v4
	v_ashrrev_i32_e32 v51, 31, v50
	v_ashrrev_i32_e32 v53, 31, v52
	v_add_u32_e32 v54, 18, v4
	v_add_u32_e32 v56, 19, v4
	v_add_u32_e32 v58, 20, v4
	v_add_u32_e32 v60, 21, v4
	v_add_u32_e32 v62, 22, v4
	v_add_u32_e32 v70, 23, v4
	v_lshlrev_b64 v[50:51], 7, v[50:51]
	v_lshlrev_b64 v[52:53], 7, v[52:53]
	v_ashrrev_i32_e32 v55, 31, v54
	v_ashrrev_i32_e32 v57, 31, v56
	v_ashrrev_i32_e32 v59, 31, v58
	v_ashrrev_i32_e32 v61, 31, v60
	v_ashrrev_i32_e32 v63, 31, v62
	v_ashrrev_i32_e32 v71, 31, v70
	v_lshl_add_u64 v[50:51], v[2:3], 0, v[50:51]
	v_lshl_add_u64 v[52:53], v[2:3], 0, v[52:53]
	v_lshlrev_b64 v[54:55], 7, v[54:55]
	v_lshlrev_b64 v[56:57], 7, v[56:57]
	v_lshlrev_b64 v[58:59], 7, v[58:59]
	v_lshlrev_b64 v[60:61], 7, v[60:61]
	v_lshlrev_b64 v[62:63], 7, v[62:63]
	v_lshlrev_b64 v[70:71], 7, v[70:71]
	v_lshl_add_u64 v[54:55], v[2:3], 0, v[54:55]
	v_lshl_add_u64 v[56:57], v[2:3], 0, v[56:57]
	v_lshl_add_u64 v[58:59], v[2:3], 0, v[58:59]
	v_lshl_add_u64 v[60:61], v[2:3], 0, v[60:61]
	v_lshl_add_u64 v[62:63], v[2:3], 0, v[62:63]
	v_lshl_add_u64 v[70:71], v[2:3], 0, v[70:71]
	global_load_dword v72, v[50:51], off
	global_load_dword v73, v[52:53], off
	global_load_dword v74, v[54:55], off
	global_load_dword v75, v[56:57], off
	global_load_dword v76, v[58:59], off
	global_load_dword v77, v[60:61], off
	global_load_dword v78, v[62:63], off
	global_load_dword v79, v[70:71], off
	v_ashrrev_i32_e32 v5, 31, v4
	v_or_b32_e32 v52, 1, v4
	v_lshlrev_b64 v[50:51], 7, v[4:5]
	v_ashrrev_i32_e32 v53, 31, v52
	v_lshl_add_u64 v[50:51], v[2:3], 0, v[50:51]
	v_lshlrev_b64 v[52:53], 7, v[52:53]
	v_lshl_add_u64 v[52:53], v[2:3], 0, v[52:53]
	global_load_dword v80, v[50:51], off
	global_load_dword v81, v[52:53], off
	v_or_b32_e32 v50, 2, v4
	v_ashrrev_i32_e32 v51, 31, v50
	v_or_b32_e32 v52, 3, v4
	v_or_b32_e32 v54, 4, v4
	v_or_b32_e32 v56, 5, v4
	v_lshlrev_b64 v[50:51], 7, v[50:51]
	v_ashrrev_i32_e32 v53, 31, v52
	v_ashrrev_i32_e32 v55, 31, v54
	v_ashrrev_i32_e32 v57, 31, v56
	v_lshl_add_u64 v[50:51], v[2:3], 0, v[50:51]
	v_lshlrev_b64 v[52:53], 7, v[52:53]
	v_lshlrev_b64 v[54:55], 7, v[54:55]
	v_lshlrev_b64 v[56:57], 7, v[56:57]
	v_lshl_add_u64 v[52:53], v[2:3], 0, v[52:53]
	v_lshl_add_u64 v[54:55], v[2:3], 0, v[54:55]
	v_lshl_add_u64 v[56:57], v[2:3], 0, v[56:57]
	global_load_dword v84, v[50:51], off
	global_load_dword v85, v[52:53], off
	global_load_dword v88, v[54:55], off
	global_load_dword v89, v[56:57], off
	v_or_b32_e32 v50, 6, v4
	v_ashrrev_i32_e32 v51, 31, v50
	v_or_b32_e32 v4, 7, v4
	v_lshlrev_b64 v[50:51], 7, v[50:51]
	v_ashrrev_i32_e32 v5, 31, v4
	v_lshl_add_u64 v[50:51], v[2:3], 0, v[50:51]
	v_lshlrev_b64 v[4:5], 7, v[4:5]
	v_lshl_add_u64 v[2:3], v[2:3], 0, v[4:5]
	global_load_dword v4, v[50:51], off
	global_load_dword v5, v[2:3], off
	s_waitcnt vmcnt(32)
	v_cvt_pk_bf16_f32 v45, v6, v7
	v_lshlrev_b32_e32 v2, 16, v45
	v_and_b32_e32 v3, 0xffff0000, v45
	v_pk_add_f32 v[2:3], v[6:7], v[2:3] neg_lo:[0,1] neg_hi:[0,1]
	s_waitcnt vmcnt(30)
	v_cvt_pk_bf16_f32 v50, v14, v15
	v_cvt_pk_bf16_f32 v49, v2, v3
	v_lshlrev_b32_e32 v2, 16, v50
	v_and_b32_e32 v3, 0xffff0000, v50
	v_pk_add_f32 v[2:3], v[14:15], v[2:3] neg_lo:[0,1] neg_hi:[0,1]
	s_waitcnt vmcnt(28)
	v_cvt_pk_bf16_f32 v51, v12, v13
	v_cvt_pk_bf16_f32 v54, v2, v3
	v_lshlrev_b32_e32 v2, 16, v51
	v_and_b32_e32 v3, 0xffff0000, v51
	v_pk_add_f32 v[2:3], v[12:13], v[2:3] neg_lo:[0,1] neg_hi:[0,1]
	s_waitcnt vmcnt(26)
	v_cvt_pk_bf16_f32 v52, v10, v11
	v_cvt_pk_bf16_f32 v55, v2, v3
	v_lshlrev_b32_e32 v2, 16, v52
	v_and_b32_e32 v3, 0xffff0000, v52
	v_pk_add_f32 v[2:3], v[10:11], v[2:3] neg_lo:[0,1] neg_hi:[0,1]
	s_waitcnt vmcnt(24)
	v_cvt_pk_bf16_f32 v53, v8, v9
	v_cvt_pk_bf16_f32 v56, v2, v3
	v_lshlrev_b32_e32 v2, 16, v53
	v_and_b32_e32 v3, 0xffff0000, v53
	v_pk_add_f32 v[2:3], v[8:9], v[2:3] neg_lo:[0,1] neg_hi:[0,1]
	s_waitcnt vmcnt(22)
	v_cvt_pk_bf16_f32 v58, v64, v65
	v_cvt_pk_bf16_f32 v57, v2, v3
	v_lshlrev_b32_e32 v2, 16, v58
	v_and_b32_e32 v3, 0xffff0000, v58
	v_pk_add_f32 v[2:3], v[64:65], v[2:3] neg_lo:[0,1] neg_hi:[0,1]
	s_waitcnt vmcnt(20)
	v_cvt_pk_bf16_f32 v59, v66, v67
	v_cvt_pk_bf16_f32 v62, v2, v3
	v_lshlrev_b32_e32 v2, 16, v59
	v_and_b32_e32 v3, 0xffff0000, v59
	v_pk_add_f32 v[2:3], v[66:67], v[2:3] neg_lo:[0,1] neg_hi:[0,1]
	s_waitcnt vmcnt(18)
	v_cvt_pk_bf16_f32 v60, v68, v69
	v_cvt_pk_bf16_f32 v63, v2, v3
	v_lshlrev_b32_e32 v2, 16, v60
	v_and_b32_e32 v3, 0xffff0000, v60
	v_pk_add_f32 v[2:3], v[68:69], v[2:3] neg_lo:[0,1] neg_hi:[0,1]
	s_waitcnt vmcnt(16)
	v_cvt_pk_bf16_f32 v61, v16, v17
	v_cvt_pk_bf16_f32 v64, v2, v3
	v_lshlrev_b32_e32 v2, 16, v61
	v_and_b32_e32 v3, 0xffff0000, v61
	v_pk_add_f32 v[2:3], v[16:17], v[2:3] neg_lo:[0,1] neg_hi:[0,1]
	s_waitcnt vmcnt(14)
	v_cvt_pk_bf16_f32 v66, v72, v73
	v_cvt_pk_bf16_f32 v65, v2, v3
	v_lshlrev_b32_e32 v2, 16, v66
	v_and_b32_e32 v3, 0xffff0000, v66
	v_pk_add_f32 v[2:3], v[72:73], v[2:3] neg_lo:[0,1] neg_hi:[0,1]
	s_waitcnt vmcnt(12)
	v_cvt_pk_bf16_f32 v67, v74, v75
	v_cvt_pk_bf16_f32 v70, v2, v3
	v_lshlrev_b32_e32 v2, 16, v67
	v_and_b32_e32 v3, 0xffff0000, v67
	v_pk_add_f32 v[2:3], v[74:75], v[2:3] neg_lo:[0,1] neg_hi:[0,1]
	s_waitcnt vmcnt(10)
	v_cvt_pk_bf16_f32 v68, v76, v77
	v_cvt_pk_bf16_f32 v71, v2, v3
	v_lshlrev_b32_e32 v2, 16, v68
	v_and_b32_e32 v3, 0xffff0000, v68
	v_pk_add_f32 v[2:3], v[76:77], v[2:3] neg_lo:[0,1] neg_hi:[0,1]
	s_waitcnt vmcnt(8)
	v_cvt_pk_bf16_f32 v69, v78, v79
	v_cvt_pk_bf16_f32 v72, v2, v3
	v_lshlrev_b32_e32 v2, 16, v69
	v_and_b32_e32 v3, 0xffff0000, v69
	v_pk_add_f32 v[2:3], v[78:79], v[2:3] neg_lo:[0,1] neg_hi:[0,1]
	s_waitcnt vmcnt(6)
	v_cvt_pk_bf16_f32 v74, v80, v81
	s_add_u32 s58, s26, 0x4e000000
	v_cvt_pk_bf16_f32 v73, v2, v3
	v_lshlrev_b32_e32 v2, 16, v74
	v_and_b32_e32 v3, 0xffff0000, v74
	s_addc_u32 s59, s27, 0
	s_lshl_b32 s4, s82, 6
	v_pk_add_f32 v[2:3], v[80:81], v[2:3] neg_lo:[0,1] neg_hi:[0,1]
	s_waitcnt vmcnt(4)
	v_cvt_pk_bf16_f32 v75, v84, v85
	s_ashr_i32 s5, s4, 31
	v_cvt_pk_bf16_f32 v78, v2, v3
	v_lshlrev_b32_e32 v2, 16, v75
	v_and_b32_e32 v3, 0xffff0000, v75
	s_lshl_b64 s[4:5], s[4:5], 2
	v_pk_add_f32 v[2:3], v[84:85], v[2:3] neg_lo:[0,1] neg_hi:[0,1]
	s_waitcnt vmcnt(2)
	v_cvt_pk_bf16_f32 v76, v88, v89
	s_add_u32 s36, s26, s4
	v_cvt_pk_bf16_f32 v79, v2, v3
	v_lshlrev_b32_e32 v2, 16, v76
	v_and_b32_e32 v3, 0xffff0000, v76
	s_addc_u32 s37, s27, s5
	s_lshl_b32 s40, s82, 10
	v_pk_add_f32 v[2:3], v[88:89], v[2:3] neg_lo:[0,1] neg_hi:[0,1]
	s_waitcnt vmcnt(0)
	v_cvt_pk_bf16_f32 v77, v4, v5
	s_ashr_i32 s41, s40, 31
	v_cvt_pk_bf16_f32 v80, v2, v3
	v_lshlrev_b32_e32 v2, 16, v77
	v_and_b32_e32 v3, 0xffff0000, v77
	s_lshl_b64 s[4:5], s[40:41], 2
	v_pk_add_f32 v[2:3], v[4:5], v[2:3] neg_lo:[0,1] neg_hi:[0,1]
	v_ashrrev_i32_e32 v195, 31, v194
	s_add_u32 s46, s38, s4
	v_cvt_pk_bf16_f32 v81, v2, v3
	v_readlane_b32 s4, v254, 53
	v_lshlrev_b64 v[2:3], 3, v[194:195]
	s_addc_u32 s47, s39, s5
	v_add_u32_e32 v10, s4, v0
	v_lshl_add_u64 v[4:5], s[26:27], 0, v[2:3]
	s_mov_b64 s[4:5], 0x26000000
	v_lshl_add_u64 v[84:85], v[4:5], 0, s[4:5]
	v_and_b32_e32 v4, 15, v194
	v_mul_u32_u24_e32 v4, 0x810, v4
	v_lshlrev_b32_e32 v5, 4, v87
	v_readlane_b32 s4, v253, 17
	v_ashrrev_i32_e32 v193, 31, v192
	v_lshlrev_b64 v[6:7], 2, v[192:193]
	v_add3_u32 v11, v5, s4, v4
	s_movk_i32 s4, 0x100
	v_cmp_gt_i32_e64 s[48:49], s4, v192
	v_lshlrev_b32_e32 v5, 2, v192
	v_readlane_b32 s4, v254, 54
	v_lshl_add_u64 v[8:9], s[36:37], 0, v[6:7]
	v_lshl_add_u64 v[6:7], s[26:27], 0, v[6:7]
	v_add_u32_e32 v172, s4, v5
	v_readlane_b32 s4, v254, 55
	v_add_u32_e32 v4, s61, v87
	s_ashr_i32 s73, s72, 31
	v_add_u32_e32 v173, s4, v5
	s_mov_b64 s[4:5], 0x1000
	v_lshl_add_u64 v[90:91], v[8:9], 0, s[4:5]
	v_readlane_b32 s4, v254, 56
	v_lshlrev_b32_e32 v13, 7, v4
	v_lshl_add_u32 v12, v87, 9, v10
	v_add_u32_e32 v174, s4, v5
	v_readlane_b32 s4, v254, 57
	v_lshlrev_b32_e32 v168, 3, v194
	v_bitop3_b32 v86, v194, 31, v194 bitop3:0xc
	v_add_u32_e32 v175, s4, v5
	s_mov_b64 s[4:5], 0x1600000
	v_lshl_add_u64 v[92:93], v[6:7], 0, s[4:5]
	s_mov_b64 s[4:5], 0x1640000
	v_lshl_add_u64 v[94:95], v[6:7], 0, s[4:5]
	s_lshl_b64 s[4:5], s[72:73], 10
	v_ashrrev_i32_e32 v5, 31, v4
	v_lshl_add_u64 v[4:5], v[4:5], 4, s[4:5]
	v_lshl_add_u64 v[4:5], v[4:5], 0, v[0:1]
	v_lshl_add_u64 v[4:5], s[26:27], 0, v[4:5]
	s_mov_b64 s[4:5], 0x1680000
	v_lshl_add_u64 v[96:97], v[4:5], 0, s[4:5]
	v_readlane_b32 s4, v254, 9
	s_add_u32 s6, s26, s4
	v_readlane_b32 s4, v254, 10
	s_addc_u32 s14, s27, s4
	s_lshl_b64 s[4:5], s[72:73], 17
	s_add_u32 s4, s6, s4
	s_addc_u32 s5, s14, s5
	v_lshl_add_u64 v[98:99], s[4:5], 0, v[2:3]
	v_readlane_b32 s4, v254, 13
	s_add_u32 s6, s26, s4
	v_readlane_b32 s4, v254, 14
	s_addc_u32 s14, s27, s4
	s_lshl_b64 s[4:5], s[72:73], 16
	s_add_u32 s4, s6, s4
	v_lshlrev_b32_e32 v0, 2, v87
	s_addc_u32 s5, s14, s5
	v_add3_u32 v0, s29, v0, v82
	v_lshl_add_u64 v[100:101], v[194:195], 2, s[4:5]
	v_readlane_b32 s4, v253, 18
	v_cmp_gt_u32_e64 s[38:39], 4, v82
	v_cmp_eq_u32_e64 s[40:41], 0, v82
	v_cmp_eq_u32_e64 s[42:43], 1, v82
	v_cmp_eq_u32_e64 s[44:45], 2, v82
	v_lshl_add_u64 v[88:89], v[194:195], 4, s[46:47]
	v_add_u32_e32 v169, 0x200, v168
	v_add_u32_e32 v170, 0x400, v168
	v_add_u32_e32 v171, 0x600, v168
	v_cmp_gt_i32_e64 s[46:47], 32, v192
	v_ashrrev_i32_e32 v176, 2, v192
	v_lshl_add_u32 v177, v0, 2, 0
	v_add_u32_e32 v178, 0, v11
	v_add_u32_e32 v179, s4, v12
	v_add_u32_e32 v180, v10, v13
	s_mov_b32 s26, s72
	global_load_dwordx4 v[234:237], v[88:89], off
	global_load_dwordx4 v[238:241], v[88:89], off offset:1024
	global_load_dwordx4 v[242:245], v[88:89], off offset:2048
	global_load_dwordx4 v[246:249], v[88:89], off offset:3072
	s_branch .LBB0_479

.LBB0_483:
	s_waitcnt vmcnt(7)
	v_and_b32_e32 v7, 0xffff0000, v102
	v_and_b32_e32 v9, 0xffff0000, v103
	v_lshlrev_b32_e32 v6, 16, v102
	v_lshlrev_b32_e32 v8, 16, v103
	v_mul_f32_e32 v0, v7, v7
	v_mul_f32_e32 v2, v9, v9
	v_fmac_f32_e32 v0, v6, v6
	v_fmac_f32_e32 v2, v8, v8
	s_waitcnt vmcnt(6)
	v_and_b32_e32 v11, 0xffff0000, v104
	v_and_b32_e32 v13, 0xffff0000, v105
	v_add_f32_e32 v0, v0, v2
	v_lshlrev_b32_e32 v10, 16, v104
	v_lshlrev_b32_e32 v12, 16, v105
	v_mul_f32_e32 v2, v11, v11
	v_mul_f32_e32 v3, v13, v13
	v_fmac_f32_e32 v2, v10, v10
	v_fmac_f32_e32 v3, v12, v12
	v_add_f32_e32 v2, v2, v3
	s_waitcnt vmcnt(5)
	v_and_b32_e32 v15, 0xffff0000, v106
	v_and_b32_e32 v17, 0xffff0000, v107
	v_add_f32_e32 v0, v2, v0
	v_lshlrev_b32_e32 v14, 16, v106
	v_lshlrev_b32_e32 v16, 16, v107
	v_mul_f32_e32 v2, v15, v15
	v_mul_f32_e32 v3, v17, v17
	v_fmac_f32_e32 v2, v14, v14
	v_fmac_f32_e32 v3, v16, v16
	v_add_f32_e32 v2, v2, v3
	v_add_f32_e32 v0, v2, v0
	s_waitcnt vmcnt(4)
	v_and_b32_e32 v165, 0xffff0000, v108
	v_and_b32_e32 v167, 0xffff0000, v109
	v_lshlrev_b32_e32 v164, 16, v108
	v_lshlrev_b32_e32 v166, 16, v109
	v_mul_f32_e32 v87, v165, v165
	v_mul_f32_e32 v124, v167, v167
	v_fmac_f32_e32 v87, v164, v164
	v_fmac_f32_e32 v124, v166, v166
	v_add_f32_e32 v87, v87, v124
	v_add_f32_e32 v0, v87, v0
	s_waitcnt vmcnt(3)
	v_and_b32_e32 v163, 0xffff0000, v112
	v_and_b32_e32 v161, 0xffff0000, v113
	v_add_f32_dpp v0, v0, v0 quad_perm:[1,0,3,2] row_mask:0xf bank_mask:0xf bound_ctrl:1
	v_lshlrev_b32_e32 v162, 16, v112
	v_lshlrev_b32_e32 v160, 16, v113
	v_add_f32_dpp v0, v0, v0 quad_perm:[2,3,0,1] row_mask:0xf bank_mask:0xf bound_ctrl:1
	s_waitcnt vmcnt(2)
	v_and_b32_e32 v151, 0xffff0000, v118
	v_and_b32_e32 v149, 0xffff0000, v119
	v_add_f32_dpp v0, v0, v0 row_half_mirror row_mask:0xf bank_mask:0xf bound_ctrl:1
	v_lshlrev_b32_e32 v150, 16, v118
	v_lshlrev_b32_e32 v148, 16, v119
	v_add_f32_dpp v0, v0, v0 row_mirror row_mask:0xf bank_mask:0xf bound_ctrl:1
	v_mov_b32_e32 v87, v0
	s_nop 1
	v_permlane16_swap_b32_e32 v0, v87
	v_add_f32_e32 v133, v0, v87
	v_mul_f32_e32 v0, v163, v163
	v_mul_f32_e32 v87, v161, v161
	v_fmac_f32_e32 v0, v162, v162
	v_fmac_f32_e32 v87, v160, v160
	v_add_f32_e32 v0, v0, v87
	v_mul_f32_e32 v87, v151, v151
	v_mul_f32_e32 v124, v149, v149
	v_fmac_f32_e32 v87, v150, v150
	v_fmac_f32_e32 v124, v148, v148
	v_add_f32_e32 v87, v87, v124
	s_waitcnt vmcnt(1)
	v_and_b32_e32 v125, 0xffff0000, v120
	v_and_b32_e32 v127, 0xffff0000, v121
	v_add_f32_e32 v0, v87, v0
	v_lshlrev_b32_e32 v124, 16, v120
	v_lshlrev_b32_e32 v126, 16, v121
	v_mul_f32_e32 v87, v125, v125
	v_mul_f32_e32 v128, v127, v127
	v_fmac_f32_e32 v87, v124, v124
	v_fmac_f32_e32 v128, v126, v126
	v_add_f32_e32 v87, v87, v128
	s_waitcnt vmcnt(0)
	v_and_b32_e32 v129, 0xffff0000, v122
	v_and_b32_e32 v131, 0xffff0000, v123
	v_add_f32_e32 v0, v87, v0
	v_lshlrev_b32_e32 v128, 16, v122
	v_lshlrev_b32_e32 v130, 16, v123
	v_mul_f32_e32 v87, v129, v129
	v_mul_f32_e32 v132, v131, v131
	v_fmac_f32_e32 v87, v128, v128
	v_fmac_f32_e32 v132, v130, v130
	v_add_f32_e32 v87, v87, v132
	v_add_f32_e32 v0, v87, v0
	v_mov_b32_e32 v135, v133
	s_nop 1
	v_permlane32_swap_b32_e32 v133, v135
	v_add_f32_dpp v0, v0, v0 quad_perm:[1,0,3,2] row_mask:0xf bank_mask:0xf bound_ctrl:1
	s_mov_b32 s4, 0x3a800000
	v_mov_b32_e32 v221, 0
	v_add_f32_dpp v0, v0, v0 quad_perm:[2,3,0,1] row_mask:0xf bank_mask:0xf bound_ctrl:1
	v_add_u32_e32 v193, s25, v170
	v_add_u32_e32 v195, s25, v171
	v_add_f32_dpp v0, v0, v0 row_half_mirror row_mask:0xf bank_mask:0xf bound_ctrl:1
	v_add_u32_e32 v222, s33, v168
	v_add_u32_e32 v223, s33, v169
	v_add_f32_dpp v0, v0, v0 row_mirror row_mask:0xf bank_mask:0xf bound_ctrl:1
	v_mov_b32_e32 v87, v0
	s_nop 1
	v_permlane16_swap_b32_e32 v0, v87
	v_add_f32_e32 v132, v0, v87
	v_mov_b32_e32 v134, v132
	s_nop 1
	v_permlane32_swap_b32_e32 v132, v134
	v_pk_add_f32 v[132:133], v[132:133], v[134:135]
	v_add_u32_e32 v230, s33, v170
	v_pk_fma_f32 v[186:187], v[132:133], s[4:5], v[190:191] op_sel_hi:[1,0,0]
	v_mov_b32_e32 v231, 0
	v_mul_f32_e32 v0, 0x4b800000, v187
	v_cmp_gt_f32_e32 vcc, s96, v187
	v_add_u32_e32 v233, s33, v171
	s_cmpk_lg_i32 s5, 0x300
	v_cndmask_b32_e32 v0, v187, v0, vcc
	v_rsq_f32_e32 v0, v0
	s_nop 0
	v_mul_f32_e32 v87, 0x45800000, v0
	v_cndmask_b32_e32 v0, v0, v87, vcc
	v_pk_mul_f32 v[132:133], v[6:7], v[0:1] op_sel_hi:[1,0]
	v_mov_b32_e32 v6, 0
	v_pk_mul_f32 v[136:137], v[234:235], v[132:133]
	v_pk_mul_f32 v[134:135], v[8:9], v[0:1] op_sel_hi:[1,0]
	v_cvt_pk_fp8_f32 v6, v136, v137
	v_pk_mul_f32 v[138:139], v[236:237], v[134:135]
	v_pk_mul_f32 v[140:141], v[10:11], v[0:1] op_sel_hi:[1,0]
	v_mov_b32_e32 v87, 0
	v_cvt_pk_fp8_f32 v6, v138, v139 op_sel:[0,0,1]
	v_pk_mul_f32 v[142:143], v[12:13], v[0:1] op_sel_hi:[1,0]
	v_pk_mul_f32 v[152:153], v[14:15], v[0:1] op_sel_hi:[1,0]
	v_pk_mul_f32 v[154:155], v[16:17], v[0:1] op_sel_hi:[1,0]
	global_store_dword v[110:111], v6, off offset:-1024
	v_pk_mul_f32 v[164:165], v[164:165], v[0:1] op_sel_hi:[1,0]
	v_pk_mul_f32 v[166:167], v[166:167], v[0:1] op_sel_hi:[1,0]
	v_mul_f32_e32 v0, 0x4b800000, v186
	v_cmp_gt_f32_e32 vcc, s96, v186
	v_cvt_pk_bf16_f32 v136, v136, v137
	v_cvt_pk_bf16_f32 v137, v138, v139
	v_cndmask_b32_e32 v0, v186, v0, vcc
	v_rsq_f32_e32 v0, v0
	v_lshlrev_b32_e32 v218, 16, v136
	v_and_b32_e32 v219, 0xffff0000, v136
	v_lshlrev_b32_e32 v220, 16, v137
	v_mul_f32_e32 v181, 0x45800000, v0
	v_cndmask_b32_e32 v0, v0, v181, vcc
	v_pk_mul_f32 v[186:187], v[162:163], v[0:1] op_sel_hi:[1,0]
	v_pk_mul_f32 v[200:201], v[160:161], v[0:1] op_sel_hi:[1,0]
	v_pk_mul_f32 v[204:205], v[150:151], v[0:1] op_sel_hi:[1,0]
	v_pk_mul_f32 v[208:209], v[148:149], v[0:1] op_sel_hi:[1,0]
	v_pk_mul_f32 v[212:213], v[124:125], v[0:1] op_sel_hi:[1,0]
	v_pk_mul_f32 v[214:215], v[126:127], v[0:1] op_sel_hi:[1,0]
	v_pk_fma_f32 v[2:3], v[234:235], v[132:133], v[218:219] neg_lo:[0,0,1] neg_hi:[0,0,1]
	v_add_u32_e32 v181, s25, v169
	v_cvt_pk_bf16_f32 v2, v2, v3
	v_pk_mul_f32 v[128:129], v[128:129], v[0:1] op_sel_hi:[1,0]
	v_pk_mul_f32 v[130:131], v[130:131], v[0:1] op_sel_hi:[1,0]
	v_pk_mul_f32 v[144:145], v[238:239], v[140:141]
	s_nop 0
	v_cvt_pk_fp8_f32 v87, v144, v145
	v_pk_mul_f32 v[146:147], v[240:241], v[142:143]
	s_nop 0
	v_cvt_pk_fp8_f32 v87, v146, v147 op_sel:[0,0,1]
	global_store_dword v[110:111], v87, off offset:-768
	v_mov_b32_e32 v87, 0
	v_pk_mul_f32 v[156:157], v[152:153], v[242:243]
	s_nop 0
	v_cvt_pk_fp8_f32 v87, v156, v157
	v_pk_mul_f32 v[158:159], v[154:155], v[244:245]
	s_nop 0
	v_cvt_pk_fp8_f32 v87, v158, v159 op_sel:[0,0,1]
	global_store_dword v[110:111], v87, off offset:-512
	v_mov_b32_e32 v87, 0
	v_pk_mul_f32 v[188:189], v[164:165], v[246:247]
	s_nop 0
	v_cvt_pk_fp8_f32 v87, v188, v189
	v_pk_mul_f32 v[196:197], v[166:167], v[248:249]
	s_nop 0
	v_cvt_pk_fp8_f32 v87, v196, v197 op_sel:[0,0,1]
	global_store_dword v[110:111], v87, off offset:-256
	v_mov_b32_e32 v87, 0
	v_pk_mul_f32 v[198:199], v[234:235], v[186:187]
	s_nop 0
	v_cvt_pk_fp8_f32 v87, v198, v199
	v_pk_mul_f32 v[202:203], v[236:237], v[200:201]
	s_nop 0
	v_cvt_pk_fp8_f32 v87, v202, v203 op_sel:[0,0,1]
	global_store_dword v[110:111], v87, off
	v_mov_b32_e32 v87, 0
	v_pk_mul_f32 v[206:207], v[238:239], v[204:205]
	s_nop 0
	v_cvt_pk_fp8_f32 v87, v206, v207
	v_pk_mul_f32 v[210:211], v[240:241], v[208:209]
	s_nop 0
	v_cvt_pk_fp8_f32 v87, v210, v211 op_sel:[0,0,1]
	global_store_dword v[110:111], v87, off offset:256
	v_add_u32_e32 v87, s25, v168
	ds_write_b64 v87, v[136:137]
	v_pk_mul_f32 v[216:217], v[212:213], v[242:243]
	s_nop 0
	v_cvt_pk_fp8_f32 v221, v216, v217
	v_pk_mul_f32 v[138:139], v[214:215], v[244:245]
	s_nop 0
	v_cvt_pk_fp8_f32 v221, v138, v139 op_sel:[0,0,1]
	global_store_dword v[110:111], v221, off offset:512
	v_and_b32_e32 v221, 0xffff0000, v137
	v_pk_fma_f32 v[4:5], v[236:237], v[134:135], v[220:221] neg_lo:[0,0,1] neg_hi:[0,0,1]
	s_nop 0
	v_cvt_pk_bf16_f32 v3, v4, v5
	ds_write_b64 v87, v[2:3] offset:33024
	v_cvt_pk_bf16_f32 v2, v144, v145
	v_cvt_pk_bf16_f32 v3, v146, v147
	v_lshlrev_b32_e32 v4, 16, v2
	v_and_b32_e32 v5, 0xffff0000, v2
	v_lshlrev_b32_e32 v132, 16, v3
	v_and_b32_e32 v133, 0xffff0000, v3
	ds_write_b64 v181, v[2:3]
	v_pk_fma_f32 v[2:3], v[238:239], v[140:141], v[4:5] neg_lo:[0,0,1] neg_hi:[0,0,1]
	v_pk_fma_f32 v[4:5], v[240:241], v[142:143], v[132:133] neg_lo:[0,0,1] neg_hi:[0,0,1]
	v_cvt_pk_bf16_f32 v2, v2, v3
	v_cvt_pk_bf16_f32 v3, v4, v5
	ds_write_b64 v181, v[2:3] offset:33024
	v_cvt_pk_bf16_f32 v2, v156, v157
	v_cvt_pk_bf16_f32 v3, v158, v159
	v_lshlrev_b32_e32 v4, 16, v2
	v_and_b32_e32 v5, 0xffff0000, v2
	v_lshlrev_b32_e32 v6, 16, v3
	v_and_b32_e32 v7, 0xffff0000, v3
	ds_write_b64 v193, v[2:3]
	v_pk_fma_f32 v[2:3], v[152:153], v[242:243], v[4:5] neg_lo:[0,0,1] neg_hi:[0,0,1]
	v_pk_fma_f32 v[4:5], v[154:155], v[244:245], v[6:7] neg_lo:[0,0,1] neg_hi:[0,0,1]
	v_cvt_pk_bf16_f32 v2, v2, v3
	v_cvt_pk_bf16_f32 v3, v4, v5
	ds_write_b64 v193, v[2:3] offset:33024
	v_cvt_pk_bf16_f32 v2, v188, v189
	v_cvt_pk_bf16_f32 v3, v196, v197
	v_lshlrev_b32_e32 v4, 16, v2
	v_and_b32_e32 v5, 0xffff0000, v2
	v_lshlrev_b32_e32 v6, 16, v3
	v_and_b32_e32 v7, 0xffff0000, v3
	ds_write_b64 v195, v[2:3]
	v_pk_fma_f32 v[2:3], v[164:165], v[246:247], v[4:5] neg_lo:[0,0,1] neg_hi:[0,0,1]
	v_pk_fma_f32 v[4:5], v[166:167], v[248:249], v[6:7] neg_lo:[0,0,1] neg_hi:[0,0,1]
	v_cvt_pk_bf16_f32 v2, v2, v3
	v_cvt_pk_bf16_f32 v3, v4, v5
	ds_write_b64 v195, v[2:3] offset:33024
	v_cvt_pk_bf16_f32 v2, v198, v199
	v_cvt_pk_bf16_f32 v3, v202, v203
	v_lshlrev_b32_e32 v4, 16, v2
	v_and_b32_e32 v5, 0xffff0000, v2
	v_lshlrev_b32_e32 v6, 16, v3
	v_and_b32_e32 v7, 0xffff0000, v3
	ds_write_b64 v222, v[2:3]
	v_pk_fma_f32 v[2:3], v[234:235], v[186:187], v[4:5] neg_lo:[0,0,1] neg_hi:[0,0,1]
	v_pk_fma_f32 v[4:5], v[236:237], v[200:201], v[6:7] neg_lo:[0,0,1] neg_hi:[0,0,1]
	v_cvt_pk_bf16_f32 v2, v2, v3
	v_cvt_pk_bf16_f32 v3, v4, v5
	ds_write_b64 v222, v[2:3] offset:33024
	v_cvt_pk_bf16_f32 v2, v206, v207
	v_cvt_pk_bf16_f32 v3, v210, v211
	v_lshlrev_b32_e32 v4, 16, v2
	v_and_b32_e32 v5, 0xffff0000, v2
	v_lshlrev_b32_e32 v6, 16, v3
	v_and_b32_e32 v7, 0xffff0000, v3
	ds_write_b64 v223, v[2:3]
	v_pk_fma_f32 v[2:3], v[238:239], v[204:205], v[4:5] neg_lo:[0,0,1] neg_hi:[0,0,1]
	v_pk_fma_f32 v[4:5], v[240:241], v[208:209], v[6:7] neg_lo:[0,0,1] neg_hi:[0,0,1]
	v_cvt_pk_bf16_f32 v2, v2, v3
	v_cvt_pk_bf16_f32 v3, v4, v5
	ds_write_b64 v223, v[2:3] offset:33024
	v_cvt_pk_bf16_f32 v2, v216, v217
	v_cvt_pk_bf16_f32 v3, v138, v139
	v_lshlrev_b32_e32 v4, 16, v2
	v_and_b32_e32 v5, 0xffff0000, v2
	v_lshlrev_b32_e32 v6, 16, v3
	v_and_b32_e32 v7, 0xffff0000, v3
	ds_write_b64 v230, v[2:3]
	v_pk_fma_f32 v[2:3], v[212:213], v[242:243], v[4:5] neg_lo:[0,0,1] neg_hi:[0,0,1]
	v_pk_fma_f32 v[4:5], v[214:215], v[244:245], v[6:7] neg_lo:[0,0,1] neg_hi:[0,0,1]
	v_cvt_pk_bf16_f32 v2, v2, v3
	v_cvt_pk_bf16_f32 v3, v4, v5
	ds_write_b64 v230, v[2:3] offset:33024
	v_pk_mul_f32 v[4:5], v[128:129], v[246:247]
	s_nop 0
	v_cvt_pk_fp8_f32 v231, v4, v5
	v_pk_mul_f32 v[2:3], v[130:131], v[248:249]
	v_cvt_pk_bf16_f32 v4, v4, v5
	v_cvt_pk_bf16_f32 v5, v2, v3
	v_cvt_pk_fp8_f32 v231, v2, v3 op_sel:[0,0,1]
	v_lshlrev_b32_e32 v6, 16, v4
	v_and_b32_e32 v7, 0xffff0000, v4
	v_lshlrev_b32_e32 v8, 16, v5
	v_and_b32_e32 v9, 0xffff0000, v5
	ds_write_b64 v233, v[4:5]
	v_pk_fma_f32 v[4:5], v[128:129], v[246:247], v[6:7] neg_lo:[0,0,1] neg_hi:[0,0,1]
	v_pk_fma_f32 v[2:3], v[130:131], v[248:249], v[8:9] neg_lo:[0,0,1] neg_hi:[0,0,1]
	v_cvt_pk_bf16_f32 v4, v4, v5
	v_cvt_pk_bf16_f32 v5, v2, v3
	global_store_dword v[110:111], v231, off offset:768
	ds_write_b64 v233, v[4:5] offset:33024
	s_cbranch_scc0 .LBB0_485
	global_load_dwordx2 v[102:103], v[114:115], off offset:-2048 nt
	global_load_dwordx2 v[104:105], v[114:115], off offset:-1536 nt
	global_load_dwordx2 v[106:107], v[114:115], off offset:-1024 nt
	global_load_dwordx2 v[108:109], v[114:115], off offset:-512 nt
	global_load_dwordx2 v[112:113], v[114:115], off nt
	global_load_dwordx2 v[118:119], v[114:115], off offset:512 nt
	global_load_dwordx2 v[120:121], v[114:115], off offset:1024 nt
	global_load_dwordx2 v[122:123], v[114:115], off offset:1536 nt
.LBB0_485:
	s_waitcnt lgkmcnt(0)
	s_barrier
	v_add_u32_e32 v0, 0x400, v179
	ds_read_b128 v[128:131], v178
	ds_read_b128 v[132:135], v178 offset:33024
	ds_read_b128 v[136:139], v178 offset:32
	ds_read_b128 v[140:143], v178 offset:33056
	ds_read_b128 v[144:147], v178 offset:64
	ds_read_b128 v[148:151], v178 offset:33088
	ds_read_b128 v[152:155], v178 offset:96
	ds_read_b128 v[156:159], v178 offset:33120
	s_waitcnt lgkmcnt(7)
	v_mfma_f32_32x32x16_bf16 v[2:17], v[128:131], v[74:77], 0
	v_mfma_f32_32x32x16_bf16 v[2:17], v[128:131], v[78:81], v[2:17]
	ds_read_b128 v[128:131], v178 offset:128
	s_waitcnt lgkmcnt(7)
	v_mfma_f32_32x32x16_bf16 v[2:17], v[132:135], v[74:77], v[2:17]
	ds_read_b128 v[132:135], v178 offset:33152
	s_waitcnt lgkmcnt(7)
	v_mfma_f32_32x32x16_bf16 v[2:17], v[136:139], v[66:69], v[2:17]
	v_mfma_f32_32x32x16_bf16 v[2:17], v[136:139], v[70:73], v[2:17]
	ds_read_b128 v[136:139], v178 offset:160
	s_waitcnt lgkmcnt(7)
	v_mfma_f32_32x32x16_bf16 v[2:17], v[140:143], v[66:69], v[2:17]
	ds_read_b128 v[140:143], v178 offset:33184
	s_waitcnt lgkmcnt(7)
	v_mfma_f32_32x32x16_bf16 v[2:17], v[144:147], v[58:61], v[2:17]
	v_mfma_f32_32x32x16_bf16 v[2:17], v[144:147], v[62:65], v[2:17]
	ds_read_b128 v[144:147], v178 offset:192
	s_waitcnt lgkmcnt(7)
	v_mfma_f32_32x32x16_bf16 v[2:17], v[148:151], v[58:61], v[2:17]
	ds_read_b128 v[148:151], v178 offset:33216
	s_waitcnt lgkmcnt(7)
	v_mfma_f32_32x32x16_bf16 v[2:17], v[152:155], v[50:53], v[2:17]
	v_mfma_f32_32x32x16_bf16 v[2:17], v[152:155], v[54:57], v[2:17]
	ds_read_b128 v[152:155], v178 offset:224
	s_waitcnt lgkmcnt(7)
	v_mfma_f32_32x32x16_bf16 v[2:17], v[156:159], v[50:53], v[2:17]
	ds_read_b128 v[156:159], v178 offset:33248
	s_waitcnt lgkmcnt(7)
	v_mfma_f32_32x32x16_bf16 v[2:17], v[128:131], v[42:45], v[2:17]
	v_mfma_f32_32x32x16_bf16 v[2:17], v[128:131], v[46:49], v[2:17]
	s_waitcnt lgkmcnt(6)
	v_mfma_f32_32x32x16_bf16 v[2:17], v[132:135], v[42:45], v[2:17]
	s_waitcnt lgkmcnt(5)
	v_mfma_f32_32x32x16_bf16 v[2:17], v[136:139], v[34:37], v[2:17]
	v_mfma_f32_32x32x16_bf16 v[2:17], v[136:139], v[38:41], v[2:17]
	s_waitcnt lgkmcnt(4)
	v_mfma_f32_32x32x16_bf16 v[2:17], v[140:143], v[34:37], v[2:17]
	s_waitcnt lgkmcnt(3)
	v_mfma_f32_32x32x16_bf16 v[2:17], v[144:147], v[26:29], v[2:17]
	v_mfma_f32_32x32x16_bf16 v[2:17], v[144:147], v[30:33], v[2:17]
	s_waitcnt lgkmcnt(2)
	v_mfma_f32_32x32x16_bf16 v[2:17], v[148:151], v[26:29], v[2:17]
	s_waitcnt lgkmcnt(1)
	v_mfma_f32_32x32x16_bf16 v[2:17], v[152:155], v[18:21], v[2:17]
	v_mfma_f32_32x32x16_bf16 v[2:17], v[152:155], v[22:25], v[2:17]
	s_waitcnt lgkmcnt(0)
	v_mfma_f32_32x32x16_bf16 v[2:17], v[156:159], v[18:21], v[2:17]
	s_nop 11
	ds_write2_b32 v179, v2, v3 offset1:32
	ds_write2_b32 v179, v4, v5 offset0:64 offset1:96
	ds_write2_b32 v0, v6, v7 offset1:32
	ds_write2_b32 v0, v8, v9 offset0:64 offset1:96
	s_waitcnt lgkmcnt(0)
	s_barrier
	ds_read2st64_b32 v[2:3], v180 offset1:8
	ds_read2st64_b32 v[4:5], v180 offset0:16 offset1:24
	ds_read2st64_b32 v[6:7], v180 offset0:32 offset1:40
	ds_read2st64_b32 v[8:9], v180 offset0:48 offset1:56
	v_mov_b32_dpp v124, v86 quad_perm:[1,0,3,2] row_mask:0xf bank_mask:0xf bound_ctrl:1
	s_waitcnt lgkmcnt(3)
	v_add_f32_e32 v0, v83, v2
	v_add_f32_e32 v0, v0, v3
	s_waitcnt lgkmcnt(2)
	v_add_f32_e32 v0, v0, v4
	v_add_f32_e32 v0, v0, v5
	s_waitcnt lgkmcnt(1)
	v_add_f32_e32 v0, v0, v6
	v_add_f32_e32 v0, v0, v7
	s_waitcnt lgkmcnt(0)
	v_add_f32_e32 v0, v0, v8
	v_add_f32_e32 v0, v0, v9
	v_add_f32_e32 v0, 0, v0
	v_not_b32_e32 v2, v0
	v_or_b32_e32 v3, 0x80000000, v0
	v_cmp_gt_i32_e32 vcc, 0, v0
	s_nop 1
	v_cndmask_b32_e32 v87, v3, v2, vcc
	s_nop 1
	v_mov_b32_dpp v125, v87 quad_perm:[1,0,3,2] row_mask:0xf bank_mask:0xf bound_ctrl:1
	v_cmp_gt_u64_e32 vcc, v[124:125], v[86:87]
	s_nop 1
	v_cndmask_b32_e32 v3, v87, v125, vcc
	v_cndmask_b32_e32 v2, v86, v124, vcc
	s_nop 0
	v_mov_b32_dpp v5, v3 quad_perm:[2,3,0,1] row_mask:0xf bank_mask:0xf bound_ctrl:1
	v_mov_b32_dpp v4, v2 quad_perm:[2,3,0,1] row_mask:0xf bank_mask:0xf bound_ctrl:1
	v_cmp_gt_u64_e32 vcc, v[4:5], v[2:3]
	s_nop 1
	v_cndmask_b32_e32 v3, v3, v5, vcc
	v_cndmask_b32_e32 v2, v2, v4, vcc
	s_nop 0
	v_mov_b32_dpp v5, v3 row_half_mirror row_mask:0xf bank_mask:0xf bound_ctrl:1
	v_mov_b32_dpp v4, v2 row_half_mirror row_mask:0xf bank_mask:0xf bound_ctrl:1
	v_cmp_gt_u64_e32 vcc, v[4:5], v[2:3]
	s_nop 1
	v_cndmask_b32_e32 v3, v3, v5, vcc
	v_cndmask_b32_e32 v2, v2, v4, vcc
	s_nop 0
	v_mov_b32_dpp v5, v3 row_mirror row_mask:0xf bank_mask:0xf bound_ctrl:1
	v_mov_b32_dpp v4, v2 row_mirror row_mask:0xf bank_mask:0xf bound_ctrl:1
	v_cmp_gt_u64_e32 vcc, v[4:5], v[2:3]
	s_nop 1
	v_cndmask_b32_e32 v2, v2, v4, vcc
	v_cndmask_b32_e32 v3, v3, v5, vcc
	v_mov_b32_e32 v4, v2
	v_mov_b32_e32 v5, v3
	s_nop 0
	v_permlane16_swap_b32_e32 v2, v4
	v_permlane16_swap_b32_e32 v3, v5
	v_cmp_gt_u64_e32 vcc, v[4:5], v[2:3]
	s_nop 1
	v_cndmask_b32_e32 v2, v2, v4, vcc
	v_sub_u32_e32 v14, 31, v2
	v_cmp_ne_u32_e64 s[50:51], v82, v14
	s_nop 1
	v_cndmask_b32_e64 v87, 0, v87, s[50:51]
	s_nop 1
	v_mov_b32_dpp v125, v87 quad_perm:[1,0,3,2] row_mask:0xf bank_mask:0xf bound_ctrl:1
	v_cmp_gt_u64_e64 s[50:51], v[124:125], v[86:87]
	s_nop 1
	v_cndmask_b32_e64 v7, v87, v125, s[50:51]
	v_cndmask_b32_e64 v6, v86, v124, s[50:51]
	s_nop 0
	v_mov_b32_dpp v9, v7 quad_perm:[2,3,0,1] row_mask:0xf bank_mask:0xf bound_ctrl:1
	v_mov_b32_dpp v8, v6 quad_perm:[2,3,0,1] row_mask:0xf bank_mask:0xf bound_ctrl:1
	v_cmp_gt_u64_e64 s[50:51], v[8:9], v[6:7]
	s_nop 1
	v_cndmask_b32_e64 v7, v7, v9, s[50:51]
	v_cndmask_b32_e64 v6, v6, v8, s[50:51]
	s_nop 0
	v_mov_b32_dpp v9, v7 row_half_mirror row_mask:0xf bank_mask:0xf bound_ctrl:1
	v_mov_b32_dpp v8, v6 row_half_mirror row_mask:0xf bank_mask:0xf bound_ctrl:1
	v_cmp_gt_u64_e64 s[50:51], v[8:9], v[6:7]
	s_nop 1
	v_cndmask_b32_e64 v7, v7, v9, s[50:51]
	v_cndmask_b32_e64 v6, v6, v8, s[50:51]
	s_nop 0
	v_mov_b32_dpp v9, v7 row_mirror row_mask:0xf bank_mask:0xf bound_ctrl:1
	v_mov_b32_dpp v8, v6 row_mirror row_mask:0xf bank_mask:0xf bound_ctrl:1
	v_cmp_gt_u64_e64 s[50:51], v[8:9], v[6:7]
	s_nop 1
	v_cndmask_b32_e64 v6, v6, v8, s[50:51]
	v_cndmask_b32_e64 v7, v7, v9, s[50:51]
	v_mov_b32_e32 v8, v6
	v_mov_b32_e32 v9, v7
	s_nop 0
	v_permlane16_swap_b32_e32 v6, v8
	v_permlane16_swap_b32_e32 v7, v9
	v_cmp_gt_u64_e64 s[50:51], v[8:9], v[6:7]
	s_nop 1
	v_cndmask_b32_e64 v4, v6, v8, s[50:51]
	v_sub_u32_e32 v15, 31, v4
	v_cmp_ne_u32_e64 s[52:53], v82, v15
	s_nop 1
	v_cndmask_b32_e64 v87, 0, v87, s[52:53]
	s_nop 1
	v_mov_b32_dpp v125, v87 quad_perm:[1,0,3,2] row_mask:0xf bank_mask:0xf bound_ctrl:1
	v_cmp_gt_u64_e64 s[52:53], v[124:125], v[86:87]
	s_nop 1
	v_cndmask_b32_e64 v11, v87, v125, s[52:53]
	v_cndmask_b32_e64 v10, v86, v124, s[52:53]
	s_nop 0
	v_mov_b32_dpp v13, v11 quad_perm:[2,3,0,1] row_mask:0xf bank_mask:0xf bound_ctrl:1
	v_mov_b32_dpp v12, v10 quad_perm:[2,3,0,1] row_mask:0xf bank_mask:0xf bound_ctrl:1
	v_cmp_gt_u64_e64 s[52:53], v[12:13], v[10:11]
	s_nop 1
	v_cndmask_b32_e64 v11, v11, v13, s[52:53]
	v_cndmask_b32_e64 v10, v10, v12, s[52:53]
	s_nop 0
	v_mov_b32_dpp v13, v11 row_half_mirror row_mask:0xf bank_mask:0xf bound_ctrl:1
	v_mov_b32_dpp v12, v10 row_half_mirror row_mask:0xf bank_mask:0xf bound_ctrl:1
	v_cmp_gt_u64_e64 s[52:53], v[12:13], v[10:11]
	s_nop 1
	v_cndmask_b32_e64 v11, v11, v13, s[52:53]
	v_cndmask_b32_e64 v10, v10, v12, s[52:53]
	s_nop 0
	v_mov_b32_dpp v13, v11 row_mirror row_mask:0xf bank_mask:0xf bound_ctrl:1
	v_mov_b32_dpp v12, v10 row_mirror row_mask:0xf bank_mask:0xf bound_ctrl:1
	v_cmp_gt_u64_e64 s[52:53], v[12:13], v[10:11]
	s_nop 1
	v_cndmask_b32_e64 v10, v10, v12, s[52:53]
	v_cndmask_b32_e64 v11, v11, v13, s[52:53]
	v_mov_b32_e32 v12, v10
	v_mov_b32_e32 v13, v11
	s_nop 0
	v_permlane16_swap_b32_e32 v10, v12
	v_permlane16_swap_b32_e32 v11, v13
	v_cmp_gt_u64_e64 s[52:53], v[12:13], v[10:11]
	s_nop 1
	v_cndmask_b32_e64 v6, v10, v12, s[52:53]
	v_sub_u32_e32 v16, 31, v6
	v_cmp_ne_u32_e64 s[54:55], v82, v16
	s_nop 1
	v_cndmask_b32_e64 v87, 0, v87, s[54:55]
	s_nop 1
	v_mov_b32_dpp v125, v87 quad_perm:[1,0,3,2] row_mask:0xf bank_mask:0xf bound_ctrl:1
	v_cmp_gt_u64_e64 s[54:55], v[124:125], v[86:87]
	s_nop 1
	v_cndmask_b32_e64 v125, v87, v125, s[54:55]
	v_cndmask_b32_e64 v124, v86, v124, s[54:55]
	s_nop 0
	v_mov_b32_dpp v127, v125 quad_perm:[2,3,0,1] row_mask:0xf bank_mask:0xf bound_ctrl:1
	v_mov_b32_dpp v126, v124 quad_perm:[2,3,0,1] row_mask:0xf bank_mask:0xf bound_ctrl:1
	v_cmp_gt_u64_e64 s[54:55], v[126:127], v[124:125]
	s_nop 1
	v_cndmask_b32_e64 v125, v125, v127, s[54:55]
	v_cndmask_b32_e64 v124, v124, v126, s[54:55]
	s_nop 0
	v_mov_b32_dpp v127, v125 row_half_mirror row_mask:0xf bank_mask:0xf bound_ctrl:1
	v_mov_b32_dpp v126, v124 row_half_mirror row_mask:0xf bank_mask:0xf bound_ctrl:1
	v_cmp_gt_u64_e64 s[54:55], v[126:127], v[124:125]
	s_nop 1
	v_cndmask_b32_e64 v125, v125, v127, s[54:55]
	v_cndmask_b32_e64 v124, v124, v126, s[54:55]
	s_nop 0
	v_mov_b32_dpp v127, v125 row_mirror row_mask:0xf bank_mask:0xf bound_ctrl:1
	v_mov_b32_dpp v126, v124 row_mirror row_mask:0xf bank_mask:0xf bound_ctrl:1
	v_cmp_gt_u64_e64 s[54:55], v[126:127], v[124:125]
	s_nop 1
	v_cndmask_b32_e64 v8, v124, v126, s[54:55]
	v_cndmask_b32_e64 v0, v125, v127, s[54:55]
	v_mov_b32_e32 v10, v8
	v_mov_b32_e32 v12, v0
	s_nop 1
	v_permlane16_swap_b32_e32 v0, v12
	v_permlane16_swap_b32_e32 v8, v10
	s_and_saveexec_b64 s[36:37], s[38:39]
	s_cbranch_execz .LBB0_482
	v_cndmask_b32_e32 v3, v3, v5, vcc
	v_cndmask_b32_e64 v5, v7, v9, s[50:51]
	v_cndmask_b32_e64 v7, v11, v13, s[52:53]
	v_mov_b32_e32 v11, v12
	v_mov_b32_e32 v9, v0
	v_cmp_gt_u64_e32 vcc, v[10:11], v[8:9]
	s_nop 1
	v_cndmask_b32_e32 v9, v0, v12, vcc
	v_cndmask_b32_e32 v8, v8, v10, vcc
	v_xor_b32_e32 v10, -1, v9
	v_cmp_gt_i64_e32 vcc, 0, v[8:9]
	v_xor_b32_e32 v0, -1, v3
	s_nop 0
	v_cndmask_b32_e64 v9, v10, |v9|, vcc
	v_cmp_gt_i64_e32 vcc, 0, v[2:3]
	s_nop 1
	v_cndmask_b32_e64 v0, v0, |v3|, vcc
	v_not_b32_e32 v3, v7
	v_cmp_gt_i64_e32 vcc, 0, v[6:7]
	v_not_b32_e32 v6, v5
	v_sub_f32_e32 v2, v9, v0
	v_cndmask_b32_e64 v3, v3, |v7|, vcc
	v_cmp_gt_i64_e32 vcc, 0, v[4:5]
	v_sub_f32_e32 v3, v3, v0
	v_mul_f32_e32 v3, 0x3fb8aa3b, v3
	v_cndmask_b32_e64 v4, v6, |v5|, vcc
	v_sub_f32_e32 v0, v4, v0
	v_mul_f32_e32 v0, 0x3fb8aa3b, v0
	v_exp_f32_e32 v0, v0
	v_mul_f32_e32 v2, 0x3fb8aa3b, v2
	v_exp_f32_e32 v3, v3
	v_exp_f32_e32 v2, v2
	v_add_f32_e32 v4, 1.0, v0
	v_add_f32_e32 v4, v4, v3
	v_add_f32_e32 v4, v4, v2
	v_div_scale_f32 v5, s[14:15], v4, v4, 1.0
	v_rcp_f32_e32 v6, v5
	v_cndmask_b32_e64 v2, v2, v3, s[44:45]
	v_cndmask_b32_e64 v0, v2, v0, s[42:43]
	v_cndmask_b32_e64 v0, v0, 1.0, s[40:41]
	v_fma_f32 v7, -v5, v6, 1.0
	v_fmac_f32_e32 v6, v7, v6
	v_div_scale_f32 v7, vcc, 1.0, v4, 1.0
	v_mul_f32_e32 v9, v7, v6
	v_fma_f32 v10, -v5, v9, v7
	v_fmac_f32_e32 v9, v10, v6
	v_fma_f32 v5, -v5, v9, v7
	v_div_fmas_f32 v5, v5, v6, v9
	v_div_fixup_f32 v4, v5, v4, 1.0
	v_sub_u32_e32 v5, 31, v8
	v_cndmask_b32_e64 v5, v5, v16, s[44:45]
	v_cndmask_b32_e64 v5, v5, v15, s[42:43]
	v_cndmask_b32_e64 v5, v5, v14, s[40:41]
	v_lshl_add_u32 v2, v5, 2, 0
	v_add_u32_e32 v2, 0x20400, v2
	ds_add_rtn_u32 v2, v2, v225
	v_add_u32_e32 v3, s5, v177
	v_mul_f32_e32 v0, v4, v0
	v_add_u32_e32 v4, 0x20500, v3
	v_add_u32_e32 v3, 0x20900, v3
	ds_write_b32 v4, v5
	s_waitcnt lgkmcnt(1)
	ds_write_b32 v3, v2
	global_store_dword v[116:117], v0, off
	s_branch .LBB0_482
